# mlp: Spart partial loads issued first with 32-bit offsets (1 VALU per load, no 64-bit address chains); DPP instead of swizzle/bpermute in mlp final reduction, stats2 and agg1 epilogue xor-4 steps
# baseline (speedup 1.0000x reference)
.Lagg_epi:
	s_and_saveexec_b64 s[32:33], s[36:37]
	v_rcp_f32_e32 v57, v14
	ds_read_b128 v[32:35], v62 offset:0
	ds_read_b128 v[36:39], v62 offset:16
	ds_read_b128 v[40:43], v62 offset:512
	ds_read_b128 v[44:47], v62 offset:528
	ds_read_b128 v[48:51], v62 offset:1024
	ds_read_b128 v[52:55], v62 offset:1040
	s_waitcnt lgkmcnt(2)
	v_mul_f32_e32 v16, v16, v57
	v_mul_f32_e32 v17, v17, v57
	v_mul_f32_e32 v18, v18, v57
	v_mul_f32_e32 v19, v19, v57
	v_mul_f32_e32 v20, v20, v57
	v_mul_f32_e32 v21, v21, v57
	v_mul_f32_e32 v22, v22, v57
	v_mul_f32_e32 v23, v23, v57
	v_fma_f32 v16, v16, v32, v40
	v_fma_f32 v17, v17, v33, v41
	v_fma_f32 v18, v18, v34, v42
	v_fma_f32 v19, v19, v35, v43
	v_fma_f32 v20, v20, v36, v44
	v_fma_f32 v21, v21, v37, v45
	v_fma_f32 v22, v22, v38, v46
	v_fma_f32 v23, v23, v39, v47
	ds_read_b128 v[32:35], v62 offset:1536
	ds_read_b128 v[36:39], v62 offset:1552
	v_mul_f32_e32 v59, 0x3fb8aa3b, v16
	v_mul_f32_e32 v60, 0x3fb8aa3b, v17
	v_mul_f32_e32 v61, 0x3fb8aa3b, v18
	v_mul_f32_e32 v67, 0x3fb8aa3b, v19
	v_exp_f32_e32 v59, v59
	v_exp_f32_e32 v60, v60
	v_exp_f32_e32 v61, v61
	v_exp_f32_e32 v67, v67
	v_add_f32_e32 v59, -1.0, v59
	v_add_f32_e32 v60, -1.0, v60
	v_add_f32_e32 v61, -1.0, v61
	v_add_f32_e32 v67, -1.0, v67
	v_med3_f32 v16, v16, v59, 0
	v_med3_f32 v17, v17, v60, 0
	v_med3_f32 v18, v18, v61, 0
	v_med3_f32 v19, v19, v67, 0
	v_cvt_f16_f32_e32 v59, v16
	v_cvt_f16_f32_e32 v60, v17
	v_cvt_f16_f32_e32 v61, v18
	v_cvt_f16_f32_e32 v67, v19
	ds_write_b16 v3, v59
	ds_write_b16 v3, v60 offset:128
	ds_write_b16 v3, v61 offset:256
	ds_write_b16 v3, v67 offset:384
	v_mul_f32_e32 v59, 0x3fb8aa3b, v20
	v_mul_f32_e32 v60, 0x3fb8aa3b, v21
	v_mul_f32_e32 v61, 0x3fb8aa3b, v22
	v_mul_f32_e32 v67, 0x3fb8aa3b, v23
	v_exp_f32_e32 v59, v59
	v_exp_f32_e32 v60, v60
	v_exp_f32_e32 v61, v61
	v_exp_f32_e32 v67, v67
	v_add_f32_e32 v59, -1.0, v59
	v_add_f32_e32 v60, -1.0, v60
	v_add_f32_e32 v61, -1.0, v61
	v_add_f32_e32 v67, -1.0, v67
	v_med3_f32 v20, v20, v59, 0
	v_med3_f32 v21, v21, v60, 0
	v_med3_f32 v22, v22, v61, 0
	v_med3_f32 v23, v23, v67, 0
	v_cvt_f16_f32_e32 v59, v20
	v_cvt_f16_f32_e32 v60, v21
	v_cvt_f16_f32_e32 v61, v22
	v_cvt_f16_f32_e32 v67, v23
	ds_write_b16 v3, v59 offset:512
	ds_write_b16 v3, v60 offset:640
	ds_write_b16 v3, v61 offset:768
	ds_write_b16 v3, v67 offset:896
	s_waitcnt lgkmcnt(0)
	v_mul_f32_e32 v56, v16, v48
	v_mul_f32_e32 v58, v16, v32
	v_fmac_f32_e32 v56, v17, v49
	v_fmac_f32_e32 v58, v17, v33
	v_fmac_f32_e32 v56, v18, v50
	v_fmac_f32_e32 v58, v18, v34
	v_fmac_f32_e32 v56, v19, v51
	v_fmac_f32_e32 v58, v19, v35
	v_fmac_f32_e32 v56, v20, v52
	v_fmac_f32_e32 v58, v20, v36
	v_fmac_f32_e32 v56, v21, v53
	v_fmac_f32_e32 v58, v21, v37
	v_fmac_f32_e32 v56, v22, v54
	v_fmac_f32_e32 v58, v22, v38
	v_fmac_f32_e32 v56, v23, v55
	v_fmac_f32_e32 v58, v23, v39
	ds_read_b128 v[32:35], v62 offset:32
	ds_read_b128 v[36:39], v62 offset:48
	ds_read_b128 v[40:43], v62 offset:544
	ds_read_b128 v[44:47], v62 offset:560
	ds_read_b128 v[48:51], v62 offset:1056
	ds_read_b128 v[52:55], v62 offset:1072
	s_waitcnt lgkmcnt(2)
	v_mul_f32_e32 v24, v24, v57
	v_mul_f32_e32 v25, v25, v57
	v_mul_f32_e32 v26, v26, v57
	v_mul_f32_e32 v27, v27, v57
	v_mul_f32_e32 v28, v28, v57
	v_mul_f32_e32 v29, v29, v57
	v_mul_f32_e32 v30, v30, v57
	v_mul_f32_e32 v31, v31, v57
	v_fma_f32 v24, v24, v32, v40
	v_fma_f32 v25, v25, v33, v41
	v_fma_f32 v26, v26, v34, v42
	v_fma_f32 v27, v27, v35, v43
	v_fma_f32 v28, v28, v36, v44
	v_fma_f32 v29, v29, v37, v45
	v_fma_f32 v30, v30, v38, v46
	v_fma_f32 v31, v31, v39, v47
	ds_read_b128 v[32:35], v62 offset:1568
	ds_read_b128 v[36:39], v62 offset:1584
	v_mul_f32_e32 v59, 0x3fb8aa3b, v24
	v_mul_f32_e32 v60, 0x3fb8aa3b, v25
	v_mul_f32_e32 v61, 0x3fb8aa3b, v26
	v_mul_f32_e32 v67, 0x3fb8aa3b, v27
	v_exp_f32_e32 v59, v59
	v_exp_f32_e32 v60, v60
	v_exp_f32_e32 v61, v61
	v_exp_f32_e32 v67, v67
	v_add_f32_e32 v59, -1.0, v59
	v_add_f32_e32 v60, -1.0, v60
	v_add_f32_e32 v61, -1.0, v61
	v_add_f32_e32 v67, -1.0, v67
	v_med3_f32 v24, v24, v59, 0
	v_med3_f32 v25, v25, v60, 0
	v_med3_f32 v26, v26, v61, 0
	v_med3_f32 v27, v27, v67, 0
	v_cvt_f16_f32_e32 v59, v24
	v_cvt_f16_f32_e32 v60, v25
	v_cvt_f16_f32_e32 v61, v26
	v_cvt_f16_f32_e32 v67, v27
	ds_write_b16 v3, v59 offset:1024
	ds_write_b16 v3, v60 offset:1152
	ds_write_b16 v3, v61 offset:1280
	ds_write_b16 v3, v67 offset:1408
	v_mul_f32_e32 v59, 0x3fb8aa3b, v28
	v_mul_f32_e32 v60, 0x3fb8aa3b, v29
	v_mul_f32_e32 v61, 0x3fb8aa3b, v30
	v_mul_f32_e32 v67, 0x3fb8aa3b, v31
	v_exp_f32_e32 v59, v59
	v_exp_f32_e32 v60, v60
	v_exp_f32_e32 v61, v61
	v_exp_f32_e32 v67, v67
	v_add_f32_e32 v59, -1.0, v59
	v_add_f32_e32 v60, -1.0, v60
	v_add_f32_e32 v61, -1.0, v61
	v_add_f32_e32 v67, -1.0, v67
	v_med3_f32 v28, v28, v59, 0
	v_med3_f32 v29, v29, v60, 0
	v_med3_f32 v30, v30, v61, 0
	v_med3_f32 v31, v31, v67, 0
	v_cvt_f16_f32_e32 v59, v28
	v_cvt_f16_f32_e32 v60, v29
	v_cvt_f16_f32_e32 v61, v30
	v_cvt_f16_f32_e32 v67, v31
	ds_write_b16 v3, v59 offset:1536
	ds_write_b16 v3, v60 offset:1664
	ds_write_b16 v3, v61 offset:1792
	ds_write_b16 v3, v67 offset:1920
	s_waitcnt lgkmcnt(0)
	v_fmac_f32_e32 v56, v24, v48
	v_fmac_f32_e32 v58, v24, v32
	v_fmac_f32_e32 v56, v25, v49
	v_fmac_f32_e32 v58, v25, v33
	v_fmac_f32_e32 v56, v26, v50
	v_fmac_f32_e32 v58, v26, v34
	v_fmac_f32_e32 v56, v27, v51
	v_fmac_f32_e32 v58, v27, v35
	v_fmac_f32_e32 v56, v28, v52
	v_fmac_f32_e32 v58, v28, v36
	v_fmac_f32_e32 v56, v29, v53
	v_fmac_f32_e32 v58, v29, v37
	v_fmac_f32_e32 v56, v30, v54
	v_fmac_f32_e32 v58, v30, v38
	v_fmac_f32_e32 v56, v31, v55
	v_fmac_f32_e32 v58, v31, v39
	s_nop 1
	v_add_f32_dpp v56, v56, v56 quad_perm:[1,0,3,2] row_mask:0xf bank_mask:0xf
	v_add_f32_dpp v58, v58, v58 quad_perm:[1,0,3,2] row_mask:0xf bank_mask:0xf
	s_nop 0
	v_add_f32_dpp v56, v56, v56 quad_perm:[2,3,0,1] row_mask:0xf bank_mask:0xf
	v_add_f32_dpp v58, v58, v58 quad_perm:[2,3,0,1] row_mask:0xf bank_mask:0xf
	s_nop 0
	v_add_f32_dpp v56, v56, v56 row_half_mirror row_mask:0xf bank_mask:0xf
	v_add_f32_dpp v58, v58, v58 row_half_mirror row_mask:0xf bank_mask:0xf
	s_and_b64 exec, exec, s[34:35]
	global_store_dword v4, v56, s[20:21]
	global_store_dword v4, v58, s[22:23]
	s_mov_b64 exec, s[32:33]
	s_waitcnt lgkmcnt(0)
	s_barrier
	ds_read_b128 v[32:35], v63
	ds_read_b128 v[36:39], v63 offset:128
	s_lshl_b32 s27, s2, 2
	s_add_i32 s27, s27, s25
	s_lshl_b32 s27, s27, 11
	v_and_b32_e32 v40, 63, v0
	v_lshlrev_b32_e32 v40, 5, v40
	v_add_u32_e32 v40, s27, v40
	s_waitcnt lgkmcnt(0)
	global_store_dwordx4 v40, v[32:35], s[18:19]
	global_store_dwordx4 v40, v[36:39], s[18:19] offset:16
	s_endpgm

.Lst2_mx_done:
	s_mov_b64 exec, -1
	s_nop 1
	v_mov_b32_dpp v23, v24 quad_perm:[1,0,3,2] row_mask:0xf bank_mask:0xf
	v_max_f32_e32 v24, v24, v23
	s_nop 1
	v_mov_b32_dpp v23, v24 quad_perm:[2,3,0,1] row_mask:0xf bank_mask:0xf
	v_max_f32_e32 v24, v24, v23
	s_nop 1
	v_max_f32_dpp v24, v24, v24 row_half_mirror row_mask:0xf bank_mask:0xf
	v_sub_f32_e32 v16, v16, v24
	v_sub_f32_e32 v17, v17, v24
	v_sub_f32_e32 v18, v18, v24
	v_sub_f32_e32 v19, v19, v24
	v_sub_f32_e32 v20, v20, v24
	v_sub_f32_e32 v21, v21, v24
	v_exp_f32_e32 v16, v16
	v_exp_f32_e32 v17, v17
	v_exp_f32_e32 v18, v18
	v_exp_f32_e32 v19, v19
	v_exp_f32_e32 v20, v20
	v_exp_f32_e32 v21, v21
	v_sub_f32_e32 v22, v22, v24
	v_add_f32_e32 v30, v16, v17
	v_add_f32_e32 v31, v18, v19
	v_add_f32_e32 v23, v20, v21
	v_add_f32_e32 v30, v30, v31
	v_add_f32_e32 v30, v30, v23
	v_add_u32_e32 v26, 48, v2
	v_add_u32_e32 v27, 192, v9

.Lst2_sm_done:
	s_mov_b64 exec, -1
	v_exp_f32_e32 v22, v22
	s_nop 1
	v_add_f32_dpp v30, v30, v30 quad_perm:[1,0,3,2] row_mask:0xf bank_mask:0xf
	s_nop 1
	v_add_f32_dpp v30, v30, v30 quad_perm:[2,3,0,1] row_mask:0xf bank_mask:0xf
	v_cmp_eq_u32_e32 vcc, 0, v2
	s_and_b64 s[18:19], s[18:19], vcc
	s_nop 0
	v_add_f32_dpp v30, v30, v30 row_half_mirror row_mask:0xf bank_mask:0xf
	v_add_f32_e32 v30, v22, v30
	v_div_scale_f32 v23, s[0:1], v30, v30, 1.0
	v_rcp_f32_e32 v26, v23
	v_div_scale_f32 v27, vcc, 1.0, v30, 1.0
	v_fma_f32 v28, -v23, v26, 1.0
	v_fmac_f32_e32 v26, v28, v26
	v_mul_f32_e32 v28, v27, v26
	v_fma_f32 v29, -v23, v28, v27
	v_fmac_f32_e32 v28, v29, v26
	v_fma_f32 v23, -v23, v28, v27
	v_div_fmas_f32 v23, v23, v26, v28
	v_div_fixup_f32 v14, v23, v30, 1.0
	v_mov_b32_e32 v12, v6
	v_mov_b32_e32 v13, v24
	v_mov_b32_e32 v15, v8
	v_lshlrev_b32_e32 v3, 4, v1
	s_and_saveexec_b64 s[0:1], s[18:19]
	global_store_dwordx4 v3, v[12:15], s[14:15]
	s_endpgm

_Z10mlp_kernelPKfPKiS0_S0_S0_S0_S0_S0_Pf:
	s_load_dwordx2 s[4:5], s[0:1], 0x0
	s_load_dwordx2 s[6:7], s[0:1], 0x10
	s_load_dwordx2 s[8:9], s[0:1], 0x20
	s_load_dwordx2 s[34:35], s[0:1], 0x8
	s_load_dwordx2 s[36:37], s[0:1], 0x18
	s_load_dwordx2 s[38:39], s[0:1], 0x28
	s_load_dwordx4 s[40:43], s[0:1], 0x30
	v_and_b32_e32 v1, 0x7f, v0
	v_lshrrev_b32_e32 v33, 7, v0
	v_lshlrev_b32_e32 v4, 2, v1
	v_lshl_or_b32 v2, v33, 13, v4
	v_mov_b32_e32 v3, 0
	v_lshl_or_b32 v58, v33, 6, s2
	v_lshl_add_u32 v58, v58, 9, v4
	v_or_b32_e32 v57, 0xc0, v33
	v_mov_b32_e32 v59, 0
	s_waitcnt lgkmcnt(0)
	s_lshl_b32 s44, s2, 2
	s_add_u32 s34, s34, s44
	s_addc_u32 s35, s35, 0
	s_load_dword s45, s[34:35], 0x0
	s_load_dword s46, s[34:35], 0x100
	s_load_dword s47, s[34:35], 0x200
	s_load_dword s48, s[34:35], 0x300
	s_load_dword s49, s[34:35], 0x400
	s_load_dword s50, s[34:35], 0x500
	s_load_dword s51, s[34:35], 0x600
	s_load_dword s52, s[34:35], 0x700
	s_load_dword s53, s[34:35], 0x800
	s_load_dword s54, s[34:35], 0x900
	s_load_dword s55, s[34:35], 0xa00
	s_load_dword s56, s[34:35], 0xb00
	s_load_dword s57, s[34:35], 0xc00
	s_load_dword s58, s[34:35], 0xd00
	s_load_dword s59, s[34:35], 0xe00
	s_load_dword s60, s[34:35], 0xf00
	s_load_dword s61, s[34:35], 0x1000
	s_load_dword s62, s[34:35], 0x1100
	s_load_dword s63, s[34:35], 0x1200
	s_load_dword s64, s[34:35], 0x1300
	s_load_dword s65, s[34:35], 0x1400
	s_load_dword s66, s[34:35], 0x1500
	s_load_dword s67, s[34:35], 0x1600
	s_load_dword s68, s[34:35], 0x1700
	s_load_dword s69, s[34:35], 0x1800
	global_load_dword v5, v58, s[4:5]
	v_add_u32_e32 v58, 0x40000, v58
	global_load_dword v34, v58, s[4:5]
	v_add_u32_e32 v58, 0x40000, v58
	global_load_dword v35, v58, s[4:5]
	v_add_u32_e32 v58, 0x40000, v58
	global_load_dword v36, v58, s[4:5]
	v_add_u32_e32 v58, 0x40000, v58
	global_load_dword v37, v58, s[4:5]
	v_add_u32_e32 v58, 0x40000, v58
	global_load_dword v38, v58, s[4:5]
	v_add_u32_e32 v58, 0x40000, v58
	global_load_dword v39, v58, s[4:5]
	v_add_u32_e32 v58, 0x40000, v58
	global_load_dword v40, v58, s[4:5]
	v_add_u32_e32 v58, 0x40000, v58
	global_load_dword v41, v58, s[4:5]
	v_add_u32_e32 v58, 0x40000, v58
	global_load_dword v42, v58, s[4:5]
	v_add_u32_e32 v58, 0x40000, v58
	global_load_dword v43, v58, s[4:5]
	v_add_u32_e32 v58, 0x40000, v58
	global_load_dword v44, v58, s[4:5]
	v_add_u32_e32 v58, 0x40000, v58
	global_load_dword v45, v58, s[4:5]
	v_add_u32_e32 v58, 0x40000, v58
	global_load_dword v46, v58, s[4:5]
	v_add_u32_e32 v58, 0x40000, v58
	global_load_dword v47, v58, s[4:5]
	v_add_u32_e32 v58, 0x40000, v58
	global_load_dword v48, v58, s[4:5]
	v_add_u32_e32 v58, 0x40000, v58
	global_load_dword v49, v58, s[4:5]
	v_add_u32_e32 v58, 0x40000, v58
	global_load_dword v50, v58, s[4:5]
	v_add_u32_e32 v58, 0x40000, v58
	global_load_dword v51, v58, s[4:5]
	v_add_u32_e32 v58, 0x40000, v58
	global_load_dword v52, v58, s[4:5]
	v_add_u32_e32 v58, 0x40000, v58
	global_load_dword v53, v58, s[4:5]
	v_add_u32_e32 v58, 0x40000, v58
	global_load_dword v54, v58, s[4:5]
	v_add_u32_e32 v58, 0x40000, v58
	global_load_dword v55, v58, s[4:5]
	v_add_u32_e32 v58, 0x40000, v58
	global_load_dword v56, v58, s[4:5]
	v_add_u32_e32 v58, 0x40000, v58
	v_cmp_gt_u32_e32 vcc, 0xc4, v57
	s_and_saveexec_b64 s[10:11], vcc
	global_load_dword v59, v58, s[4:5]
	s_mov_b64 exec, s[10:11]
	v_min_u32_e32 v64, 0x7f, v0
	v_lshlrev_b32_e32 v64, 2, v64
	global_load_dword v65, v64, s[36:37]
	v_min_u32_e32 v66, 63, v0
	v_lshlrev_b32_e32 v66, 2, v66
	global_load_dword v67, v66, s[38:39]
	v_and_b32_e32 v68, 15, v0
	v_lshrrev_b32_e32 v69, 4, v0
	v_min_u32_e32 v69, 9, v69
	v_mul_u32_u24_e32 v70, 40, v68
	v_add_lshl_u32 v70, v70, v69, 2
	global_load_dword v71, v70, s[40:41]
	global_load_dword v72, v70, s[40:41] offset:40
	global_load_dword v73, v70, s[40:41] offset:80
	global_load_dword v74, v70, s[40:41] offset:120
	v_lshlrev_b32_e32 v75, 2, v69
	global_load_dword v76, v75, s[42:43]
	v_lshl_add_u64 v[6:7], s[6:7], 0, v[2:3]
	global_load_dword v32, v2, s[6:7]
	global_load_dword v30, v2, s[6:7] offset:512
	global_load_dword v28, v2, s[6:7] offset:1024
	global_load_dword v26, v2, s[6:7] offset:1536
	global_load_dword v24, v2, s[6:7] offset:2048
	global_load_dword v22, v2, s[6:7] offset:2560
	global_load_dword v20, v2, s[6:7] offset:3072
	global_load_dword v18, v2, s[6:7] offset:3584
	s_movk_i32 s3, 0x1000
	v_and_b32_e32 v2, 63, v0
	v_add_co_u32_e32 v6, vcc, s3, v6
	v_lshrrev_b32_e32 v1, 6, v0
	v_lshlrev_b32_e32 v8, 2, v2
	v_addc_co_u32_e32 v7, vcc, 0, v7, vcc
	v_lshl_or_b32 v2, v1, 11, v8
	global_load_dword v31, v[6:7], off
	global_load_dword v29, v[6:7], off offset:512
	global_load_dword v27, v[6:7], off offset:1024
	global_load_dword v25, v[6:7], off offset:1536
	global_load_dword v23, v[6:7], off offset:2048
	global_load_dword v21, v[6:7], off offset:2560
	global_load_dword v19, v[6:7], off offset:3072
	global_load_dword v17, v[6:7], off offset:3584
	global_load_dword v16, v2, s[8:9]
	global_load_dword v15, v2, s[8:9] offset:256
	global_load_dword v14, v2, s[8:9] offset:512
	global_load_dword v13, v2, s[8:9] offset:768
	global_load_dword v12, v2, s[8:9] offset:1024
	global_load_dword v11, v2, s[8:9] offset:1280
	global_load_dword v10, v2, s[8:9] offset:1536
	global_load_dword v9, v2, s[8:9] offset:1792
	v_lshlrev_b32_e32 v2, 6, v33
	s_waitcnt vmcnt(54)
	v_add_f32_e32 v5, 0, v5
	s_waitcnt vmcnt(53)
	v_add_f32_e32 v5, v5, v34
	s_waitcnt vmcnt(52)
	v_add_f32_e32 v5, v5, v35
	s_waitcnt vmcnt(51)
	v_add_f32_e32 v5, v5, v36
	s_waitcnt vmcnt(50)
	v_add_f32_e32 v5, v5, v37
	s_waitcnt vmcnt(49)
	v_add_f32_e32 v5, v5, v38
	s_waitcnt vmcnt(48)
	v_add_f32_e32 v5, v5, v39
	s_waitcnt vmcnt(47)
	v_add_f32_e32 v5, v5, v40
	s_waitcnt vmcnt(46)
	v_add_f32_e32 v5, v5, v41
	s_waitcnt vmcnt(45)
	v_add_f32_e32 v5, v5, v42
	s_waitcnt vmcnt(44)
	v_add_f32_e32 v5, v5, v43
	s_waitcnt vmcnt(43)
	v_add_f32_e32 v5, v5, v44
	s_waitcnt vmcnt(42)
	v_add_f32_e32 v5, v5, v45
	s_waitcnt vmcnt(41)
	v_add_f32_e32 v5, v5, v46
	s_waitcnt vmcnt(40)
	v_add_f32_e32 v5, v5, v47
	s_waitcnt vmcnt(39)
	v_add_f32_e32 v5, v5, v48
	s_waitcnt vmcnt(38)
	v_add_f32_e32 v5, v5, v49
	s_waitcnt vmcnt(37)
	v_add_f32_e32 v5, v5, v50
	s_waitcnt vmcnt(36)
	v_add_f32_e32 v5, v5, v51
	s_waitcnt vmcnt(35)
	v_add_f32_e32 v5, v5, v52
	s_waitcnt vmcnt(34)
	v_add_f32_e32 v5, v5, v53
	s_waitcnt vmcnt(33)
	v_add_f32_e32 v5, v5, v54
	s_waitcnt vmcnt(32)
	v_add_f32_e32 v5, v5, v55
	s_waitcnt vmcnt(31)
	v_add_f32_e32 v5, v5, v56
	v_add_f32_e32 v3, v5, v59
	v_lshl_or_b32 v4, v33, 9, v4
	s_movk_i32 s4, 0x80
	ds_write_b32 v4, v3
	v_cmp_gt_u32_e32 vcc, s4, v0
	v_lshlrev_b32_e32 v3, 2, v0
	s_waitcnt lgkmcnt(0)
	s_barrier
	s_and_saveexec_b64 s[4:5], vcc
	s_cbranch_execz .LBB5_4
	ds_read2st64_b32 v[6:7], v3 offset1:2
	ds_read2st64_b32 v[34:35], v3 offset0:8 offset1:10
	ds_read2st64_b32 v[36:37], v3 offset0:4 offset1:6
	ds_read2st64_b32 v[38:39], v3 offset0:12 offset1:14
	s_waitcnt lgkmcnt(3)
	v_mov_b32_e32 v40, v6
	s_waitcnt lgkmcnt(2)
	v_mov_b32_e32 v41, v34
	v_mov_b32_e32 v34, v7
	v_pk_add_f32 v[6:7], v[40:41], v[34:35]
	s_waitcnt lgkmcnt(1)
	v_mov_b32_e32 v34, v36
	s_waitcnt lgkmcnt(0)
	v_mov_b32_e32 v35, v38
	v_mov_b32_e32 v38, v37
	v_pk_add_f32 v[34:35], v[34:35], v[38:39]
	s_nop 0
	v_pk_add_f32 v[6:7], v[6:7], v[34:35]
	s_nop 0
	v_add_f32_e32 v5, v6, v7
	ds_write_b32 v3, v5 offset:8192
.LBB5_4:
	s_or_b64 exec, exec, s[4:5]
	s_waitcnt lgkmcnt(0)
	s_barrier
	ds_read_b128 v[34:37], v2 offset:8192
	ds_read_b128 v[38:41], v2 offset:8208
	ds_read_b128 v[42:45], v2 offset:8224
	ds_read_b128 v[46:49], v2 offset:8240
	s_waitcnt vmcnt(0) lgkmcnt(3)
	v_fma_f32 v2, v34, v32, 0
	v_fmac_f32_e32 v2, v35, v30
	v_fmac_f32_e32 v2, v36, v28
	v_fmac_f32_e32 v2, v37, v26
	s_waitcnt lgkmcnt(2)
	v_fmac_f32_e32 v2, v38, v24
	v_fmac_f32_e32 v2, v39, v22
	v_fmac_f32_e32 v2, v40, v20
	v_fmac_f32_e32 v2, v41, v18
	s_waitcnt lgkmcnt(1)
	v_fmac_f32_e32 v2, v42, v31
	v_fmac_f32_e32 v2, v43, v29
	v_fmac_f32_e32 v2, v44, v27
	v_fmac_f32_e32 v2, v45, v25
	s_waitcnt lgkmcnt(0)
	v_fmac_f32_e32 v2, v46, v23
	v_fmac_f32_e32 v2, v47, v21
	v_fmac_f32_e32 v2, v48, v19
	v_fmac_f32_e32 v2, v49, v17
	ds_write_b32 v4, v2
	s_waitcnt lgkmcnt(0)
	s_barrier
	s_and_saveexec_b64 s[4:5], vcc
	s_cbranch_execz .LBB5_6
	ds_read2st64_b32 v[4:5], v3 offset1:2
	ds_read2st64_b32 v[6:7], v3 offset0:8 offset1:10
	ds_read2st64_b32 v[18:19], v3 offset0:4 offset1:6
	ds_read2st64_b32 v[20:21], v3 offset0:12 offset1:14
	s_waitcnt lgkmcnt(0)
	s_add_i32 s31, s45, s46
	s_add_i32 s31, s31, s47
	s_add_i32 s31, s31, s48
	s_add_i32 s31, s31, s49
	s_add_i32 s31, s31, s50
	s_add_i32 s31, s31, s51
	s_add_i32 s31, s31, s52
	s_add_i32 s31, s31, s53
	s_add_i32 s31, s31, s54
	s_add_i32 s31, s31, s55
	s_add_i32 s31, s31, s56
	s_add_i32 s31, s31, s57
	s_add_i32 s31, s31, s58
	s_add_i32 s31, s31, s59
	s_add_i32 s31, s31, s60
	s_add_i32 s31, s31, s61
	s_add_i32 s31, s31, s62
	s_add_i32 s31, s31, s63
	s_add_i32 s31, s31, s64
	s_add_i32 s31, s31, s65
	s_add_i32 s31, s31, s66
	s_add_i32 s31, s31, s67
	s_add_i32 s31, s31, s68
	s_add_i32 s31, s31, s69
	v_mov_b32_e32 v22, v4
	v_mov_b32_e32 v23, v6
	v_mov_b32_e32 v6, v5
	v_mov_b32_e32 v4, v18
	v_mov_b32_e32 v5, v20
	v_mov_b32_e32 v20, v19
	v_cvt_f32_i32_e32 v17, s31
	v_pk_add_f32 v[6:7], v[22:23], v[6:7]
	v_pk_add_f32 v[4:5], v[4:5], v[20:21]
	s_nop 0
	v_pk_add_f32 v[4:5], v[6:7], v[4:5]
	s_nop 0
	v_add_f32_e32 v4, v4, v5
	v_max_f32_e32 v5, 1.0, v17
	s_waitcnt vmcnt(0)
	v_fmac_f32_e32 v4, v65, v17
	v_div_scale_f32 v2, s[6:7], v5, v5, v4
	v_rcp_f32_e32 v6, v2
	v_div_scale_f32 v7, vcc, v4, v5, v4
	v_fma_f32 v17, -v2, v6, 1.0
	v_fmac_f32_e32 v6, v17, v6
	v_mul_f32_e32 v17, v7, v6
	v_fma_f32 v18, -v2, v17, v7
	v_fmac_f32_e32 v17, v18, v6
	v_fma_f32 v2, -v2, v17, v7
	v_div_fmas_f32 v2, v2, v6, v17
	v_div_fixup_f32 v2, v2, v5, v4
	ds_write_b32 v3, v2 offset:8704

.LBB5_10:
	s_or_b64 exec, exec, s[10:11]
	s_movk_i32 s0, 0xa0
	v_cmp_gt_u32_e32 vcc, s0, v0
	s_waitcnt lgkmcnt(0)
	s_barrier
	s_and_saveexec_b64 s[0:1], vcc
	s_cbranch_execz .LBB5_13
	v_and_b32_e32 v3, 15, v0
	v_lshl_or_b32 v1, v3, 2, 1
	v_lshrrev_b32_e32 v2, 4, v0
	v_mul_u32_u24_e32 v0, 40, v3
	v_mul_u32_u24_e32 v1, 10, v1
	v_add_lshl_u32 v0, v0, v2, 2
	v_add_lshl_u32 v1, v1, v2, 2
	v_add_u32_e32 v4, 0x50, v1
	v_mov_b32_e32 v8, v71
	v_mov_b32_e32 v9, v72
	v_mov_b32_e32 v10, v73
	v_mov_b32_e32 v11, v74
	v_lshlrev_b32_e32 v1, 4, v3
	ds_read_b128 v[4:7], v1 offset:9216
	s_waitcnt vmcnt(0) lgkmcnt(0)
	v_fma_f32 v4, v4, v8, 0
	v_fmac_f32_e32 v4, v5, v9
	v_fmac_f32_e32 v4, v6, v10
	v_fmac_f32_e32 v4, v7, v11
	s_nop 1
	v_add_f32_dpp v4, v4, v4 quad_perm:[1,0,3,2] row_mask:0xf bank_mask:0xf
	s_nop 1
	v_add_f32_dpp v4, v4, v4 quad_perm:[2,3,0,1] row_mask:0xf bank_mask:0xf
	s_nop 1
	v_add_f32_dpp v4, v4, v4 row_half_mirror row_mask:0xf bank_mask:0xf
	s_nop 1
	v_add_f32_dpp v4, v4, v4 row_mirror row_mask:0xf bank_mask:0xf
	v_cmp_eq_u32_e32 vcc, 0, v3
	s_and_b64 exec, exec, vcc
	s_cbranch_execz .LBB5_13
	v_mov_b32_e32 v3, v76
	v_mad_u64_u32 v[0:1], s[0:1], s2, 10, v[2:3]
	v_ashrrev_i32_e32 v1, 31, v0
	v_add_f32_e32 v2, v4, v3
	v_lshl_add_u64 v[0:1], v[0:1], 2, s[8:9]
	global_store_dword v[0:1], v2, off
